# P0 transpose queue: 2 items per claim instead of 8 (on top of the S5-unit and adaLN staging changes)
# speedup vs baseline: 1.0068x; 1.0068x over previous
; #define RI_NEXT(D_) do { if (q.cnt == 8) { int b_ = 0; if (F.lane == 0) b_ = (int)__hip_atomic_fetch_add(qctr, 8u, __ATOMIC_RELAXED, __HIP_MEMORY_SCOPE_AGENT); q.base = __builtin_amdgcn_readfirstlane(b_); q.cnt = 0; } \
;         D_ = decode_item(KA, F.ws, kind, q.base + q.cnt); ++q.cnt; } while (0)
; DI void run_items1(Frame& F, int kind, int quota, QState& q) {
;     ...
;     if (quota == 0) return;
;     TItem d; RI_NEXT(d); if (!d.valid) return;
.LBB0_79:
	s_mov_b32 s2, -1
	s_add_u32 s0, s46, 0x8000
	v_mbcnt_lo_u32_b32 v1, s2, 0
	v_mbcnt_hi_u32_b32 v64, s2, v1
	s_mov_b32 s2, s88
	s_addc_u32 s1, s47, 0
	v_mov_b32_e32 v0, 0
	s_mov_b64 s[2:3], s[70:71]
	v_cmp_eq_u32_e64 s[4:5], 0, v64
	s_and_saveexec_b64 s[6:7], s[4:5]
	s_cbranch_execz .LBB0_83
	s_mov_b64 s[10:11], exec
	v_mbcnt_lo_u32_b32 v0, s10, 0
	v_mbcnt_hi_u32_b32 v0, s11, v0
	v_cmp_eq_u32_e32 vcc, 0, v0
	s_and_saveexec_b64 s[8:9], vcc
	s_cbranch_execz .LBB0_82
	s_bcnt1_i32_b64 s10, s[10:11]
	s_lshl_b32 s10, s10, 1
	v_mov_b32_e32 v1, 0
	v_mov_b32_e32 v2, s10
	global_atomic_add v1, v1, v2, s[0:1] sc0
.LBB0_82:
	s_or_b64 exec, exec, s[8:9]
	s_waitcnt vmcnt(0)
	v_readfirstlane_b32 s8, v1
	s_nop 1
	v_lshl_add_u32 v0, v0, 1, s8

; #define LDS_WAIT() asm volatile("s_waitcnt lgkmcnt(0)" ::: "memory")
; DI void item_scatter(const f32x4 (&v)[16], LAS float* scr, int lane) {
;     ...
;     for (int i = 0; i < 16; ++i) { const int k = 4 * i + r4;
; #pragma unroll
;         for (int j = 0; j < 4; ++j) scr[(4 * c4 + j) * 64 + (k ^ (4 * (c4 ^ j)))] = v[i][j]; }
;     LDS_WAIT(); asm volatile("" ::: "memory");
.LBB0_95:
	s_waitcnt vmcnt(0)
	ds_write_b32 v72, v24
	ds_write_b32 v73, v25 offset:256
	ds_write_b32 v74, v26 offset:512
	ds_write_b32 v75, v27 offset:768
	ds_write_b32 v76, v0
	ds_write_b32 v77, v1 offset:256
	ds_write_b32 v78, v2 offset:512
	ds_write_b32 v79, v3 offset:768
	ds_write_b32 v80, v4
	ds_write_b32 v81, v5 offset:256
	ds_write_b32 v82, v6 offset:512
	ds_write_b32 v83, v7 offset:768
	ds_write_b32 v84, v8
	ds_write_b32 v85, v9 offset:256
	ds_write_b32 v86, v10 offset:512
	ds_write_b32 v87, v11 offset:768
	ds_write_b32 v88, v12
	ds_write_b32 v89, v13 offset:256
	ds_write_b32 v90, v14 offset:512
	ds_write_b32 v91, v15 offset:768
	ds_write_b32 v92, v16
	ds_write_b32 v93, v17 offset:256
	ds_write_b32 v94, v18 offset:512
	ds_write_b32 v95, v19 offset:768
	ds_write_b32 v96, v20
	ds_write_b32 v97, v21 offset:256
	ds_write_b32 v98, v22 offset:512
	ds_write_b32 v99, v23 offset:768
	ds_write_b32 v100, v28
	ds_write_b32 v101, v29 offset:256
	ds_write_b32 v102, v30 offset:512
	ds_write_b32 v103, v31 offset:768
	ds_write_b32 v104, v32
	ds_write_b32 v105, v33 offset:256
	ds_write_b32 v106, v34 offset:512
	ds_write_b32 v107, v35 offset:768
	ds_write_b32 v108, v36
	ds_write_b32 v109, v37 offset:256
	ds_write_b32 v110, v38 offset:512
	ds_write_b32 v111, v39 offset:768
	ds_write_b32 v112, v40
	ds_write_b32 v113, v41 offset:256
	ds_write_b32 v114, v42 offset:512
	ds_write_b32 v115, v43 offset:768
	ds_write_b32 v116, v44
	ds_write_b32 v117, v45 offset:256
	ds_write_b32 v118, v46 offset:512
	ds_write_b32 v119, v47 offset:768
	ds_write_b32 v120, v48
	ds_write_b32 v121, v49 offset:256
	ds_write_b32 v122, v50 offset:512
	ds_write_b32 v123, v51 offset:768
	ds_write_b32 v124, v52
	ds_write_b32 v125, v53 offset:256
	ds_write_b32 v126, v54 offset:512
	ds_write_b32 v127, v55 offset:768
	ds_write_b32 v128, v56
	ds_write_b32 v129, v57 offset:256
	ds_write_b32 v130, v58 offset:512
	ds_write_b32 v131, v59 offset:768
	ds_write_b32 v132, v60
	ds_write_b32 v133, v61 offset:256
	ds_write_b32 v134, v62 offset:512
	ds_write_b32 v135, v63 offset:768
	s_waitcnt lgkmcnt(0)
	s_cmp_lg_u32 s31, 2
	s_cbranch_scc1 .LBB0_101
	v_mov_b32_e32 v64, 0
	s_and_saveexec_b64 s[14:15], s[4:5]
	s_cbranch_execz .LBB0_100
	s_mov_b64 s[18:19], exec
	v_mbcnt_lo_u32_b32 v64, s18, 0
	v_mbcnt_hi_u32_b32 v64, s19, v64
	v_cmp_eq_u32_e32 vcc, 0, v64
	s_and_saveexec_b64 s[16:17], vcc
	s_cbranch_execz .LBB0_99
	s_bcnt1_i32_b64 s18, s[18:19]
	s_lshl_b32 s18, s18, 1
	v_mov_b32_e32 v65, s18
	global_atomic_add v65, v69, v65, s[0:1] sc0
.LBB0_99:
	s_or_b64 exec, exec, s[16:17]
	s_waitcnt vmcnt(0)
	v_readfirstlane_b32 s16, v65
	s_nop 1
	v_lshl_add_u32 v64, v64, 1, s16
